# P1 conversion loops: next half-item loads issue at once (dropped false WAW waits) and the common path has its own pack/store tail with vmcnt raised by the 16 younger loads, so the next loads are no lo
# speedup vs baseline: 1.0250x; 1.0081x over previous
.LBB0_292:
	v_mul_u32_u24_e32 v2, s14, v131
	v_lshlrev_b32_e32 v132, 2, v2
	v_lshl_add_u64 v[2:3], s[12:13], 0, v[132:133]
	v_lshlrev_b32_e32 v132, 2, v130
	v_lshl_add_u64 v[2:3], v[2:3], 0, v[132:133]
	s_lshl_b64 s[12:13], s[14:15], 2
	v_lshl_add_u64 v[10:11], v[2:3], 0, s[12:13]
	global_load_dwordx4 v[2:5], v[2:3], off nt
	s_nop 0
	global_load_dwordx4 v[6:9], v[10:11], off nt
	v_lshl_add_u64 v[10:11], v[10:11], 0, s[12:13]
	v_lshl_add_u64 v[18:19], v[10:11], 0, s[12:13]
	global_load_dwordx4 v[10:13], v[10:11], off nt
	s_nop 0
	global_load_dwordx4 v[14:17], v[18:19], off nt
	v_lshl_add_u64 v[18:19], v[18:19], 0, s[12:13]
	v_lshl_add_u64 v[26:27], v[18:19], 0, s[12:13]
	global_load_dwordx4 v[18:21], v[18:19], off nt
	s_nop 0
	global_load_dwordx4 v[22:25], v[26:27], off nt
	v_lshl_add_u64 v[26:27], v[26:27], 0, s[12:13]
	v_lshl_add_u64 v[28:29], v[26:27], 0, s[12:13]
	global_load_dwordx4 v[34:37], v[26:27], off nt
	global_load_dwordx4 v[42:45], v[28:29], off nt
	v_lshl_add_u64 v[26:27], v[28:29], 0, s[12:13]
	v_lshl_add_u64 v[38:39], v[26:27], 0, s[12:13]
	v_lshl_add_u64 v[46:47], v[38:39], 0, s[12:13]
	v_lshl_add_u64 v[50:51], v[46:47], 0, s[12:13]
	v_lshl_add_u64 v[54:55], v[50:51], 0, s[12:13]
	v_lshl_add_u64 v[58:59], v[54:55], 0, s[12:13]
	v_lshl_add_u64 v[62:63], v[58:59], 0, s[12:13]
	global_load_dwordx4 v[30:33], v[26:27], off nt
	s_nop 0
	global_load_dwordx4 v[26:29], v[38:39], off nt
	s_nop 0
	global_load_dwordx4 v[38:41], v[46:47], off nt
	s_nop 0
	global_load_dwordx4 v[46:49], v[50:51], off nt
	s_nop 0
	global_load_dwordx4 v[50:53], v[54:55], off nt
	s_nop 0
	global_load_dwordx4 v[54:57], v[58:59], off nt
	s_nop 0
	global_load_dwordx4 v[58:61], v[62:63], off nt
	v_lshl_add_u64 v[62:63], v[62:63], 0, s[12:13]
	global_load_dwordx4 v[62:65], v[62:63], off nt
	s_branch .Lconv_fast_0

.Lconv_fast_0:
	s_andn2_b64 vcc, exec, s[8:9]
	s_cbranch_vccnz .LBB0_238
	s_waitcnt vmcnt(31)
	v_mul_f32_e32 v132, s58, v66
	s_waitcnt vmcnt(30)
	v_mul_f32_e32 v157, s58, v70
	v_med3_f32 v132, v132, s54, v155
	v_med3_f32 v157, v157, s54, v155
	v_mov_b32_e32 v158, v133
	v_cvt_pk_fp8_f32 v158, v132, v157
	s_waitcnt vmcnt(29)
	v_mul_f32_e32 v159, s58, v74
	s_waitcnt vmcnt(28)
	v_mul_f32_e32 v132, s58, v78
	v_med3_f32 v157, v159, s54, v155
	v_med3_f32 v132, v132, s54, v155
	v_cvt_pk_fp8_f32 v158, v157, v132 op_sel:[0,0,1]
	s_waitcnt vmcnt(27)
	v_mul_f32_e32 v132, s58, v82
	s_waitcnt vmcnt(26)
	v_mul_f32_e32 v157, s58, v86
	v_med3_f32 v132, v132, s54, v155
	v_med3_f32 v157, v157, s54, v155
	v_mov_b32_e32 v159, v133
	v_cvt_pk_fp8_f32 v159, v132, v157
	s_waitcnt vmcnt(25)
	v_mul_f32_e32 v160, s58, v90
	s_waitcnt vmcnt(24)
	v_mul_f32_e32 v132, s58, v94
	v_med3_f32 v157, v160, s54, v155
	v_med3_f32 v132, v132, s54, v155
	v_cvt_pk_fp8_f32 v159, v157, v132 op_sel:[0,0,1]
	s_waitcnt vmcnt(23)
	v_mul_f32_e32 v132, s58, v98
	s_waitcnt vmcnt(22)
	v_mul_f32_e32 v157, s58, v102
	v_med3_f32 v132, v132, s54, v155
	v_med3_f32 v157, v157, s54, v155
	v_mov_b32_e32 v160, v133
	v_cvt_pk_fp8_f32 v160, v132, v157
	s_waitcnt vmcnt(21)
	v_mul_f32_e32 v161, s58, v106
	s_waitcnt vmcnt(20)
	v_mul_f32_e32 v132, s58, v110
	v_med3_f32 v157, v161, s54, v155
	v_med3_f32 v132, v132, s54, v155
	v_cvt_pk_fp8_f32 v160, v157, v132 op_sel:[0,0,1]
	s_waitcnt vmcnt(19)
	v_mul_f32_e32 v132, s58, v114
	s_waitcnt vmcnt(18)
	v_mul_f32_e32 v157, s58, v118
	v_med3_f32 v132, v132, s54, v155
	v_med3_f32 v157, v157, s54, v155
	v_mov_b32_e32 v161, v133
	v_cvt_pk_fp8_f32 v161, v132, v157
	s_waitcnt vmcnt(17)
	v_mul_f32_e32 v162, s58, v122
	s_waitcnt vmcnt(16)
	v_mul_f32_e32 v132, s58, v126
	v_med3_f32 v157, v162, s54, v155
	v_med3_f32 v132, v132, s54, v155
	v_cvt_pk_fp8_f32 v161, v157, v132 op_sel:[0,0,1]
	v_mul_f32_e32 v132, s58, v67
	v_mul_f32_e32 v157, s58, v71
	v_med3_f32 v132, v132, s54, v155
	v_med3_f32 v157, v157, s54, v155
	v_mov_b32_e32 v162, v133
	v_cvt_pk_fp8_f32 v162, v132, v157
	v_mul_f32_e32 v163, s58, v75
	v_mul_f32_e32 v132, s58, v79
	v_med3_f32 v157, v163, s54, v155
	v_med3_f32 v132, v132, s54, v155
	v_cvt_pk_fp8_f32 v162, v157, v132 op_sel:[0,0,1]
	v_mul_f32_e32 v132, s58, v83
	v_mul_f32_e32 v157, s58, v87
	v_med3_f32 v132, v132, s54, v155
	v_med3_f32 v157, v157, s54, v155
	v_mov_b32_e32 v163, v133
	v_cvt_pk_fp8_f32 v163, v132, v157
	v_mul_f32_e32 v164, s58, v91
	v_mul_f32_e32 v132, s58, v95
	v_med3_f32 v157, v164, s54, v155
	v_med3_f32 v132, v132, s54, v155
	v_cvt_pk_fp8_f32 v163, v157, v132 op_sel:[0,0,1]
	v_mul_f32_e32 v132, s58, v99
	v_mul_f32_e32 v157, s58, v103
	v_med3_f32 v132, v132, s54, v155
	v_med3_f32 v157, v157, s54, v155
	v_mov_b32_e32 v164, v133
	v_cvt_pk_fp8_f32 v164, v132, v157
	v_mul_f32_e32 v165, s58, v107
	v_mul_f32_e32 v132, s58, v111
	v_med3_f32 v157, v165, s54, v155
	v_med3_f32 v132, v132, s54, v155
	v_cvt_pk_fp8_f32 v164, v157, v132 op_sel:[0,0,1]
	v_mul_f32_e32 v132, s58, v115
	v_mul_f32_e32 v157, s58, v119
	v_med3_f32 v132, v132, s54, v155
	v_med3_f32 v157, v157, s54, v155
	v_mov_b32_e32 v165, v133
	v_cvt_pk_fp8_f32 v165, v132, v157
	v_mul_f32_e32 v166, s58, v123
	v_mul_f32_e32 v132, s58, v127
	v_med3_f32 v157, v166, s54, v155
	v_med3_f32 v132, v132, s54, v155
	v_cvt_pk_fp8_f32 v165, v157, v132 op_sel:[0,0,1]
	v_mul_f32_e32 v132, s58, v68
	v_mul_f32_e32 v157, s58, v72
	v_med3_f32 v132, v132, s54, v155
	v_med3_f32 v157, v157, s54, v155
	v_mov_b32_e32 v166, v133
	v_cvt_pk_fp8_f32 v166, v132, v157
	v_mul_f32_e32 v167, s58, v76
	v_mul_f32_e32 v132, s58, v80
	v_med3_f32 v157, v167, s54, v155
	v_med3_f32 v132, v132, s54, v155
	v_cvt_pk_fp8_f32 v166, v157, v132 op_sel:[0,0,1]
	v_mul_f32_e32 v132, s58, v84
	v_mul_f32_e32 v157, s58, v88
	v_med3_f32 v132, v132, s54, v155
	v_med3_f32 v157, v157, s54, v155
	v_mov_b32_e32 v167, v133
	v_cvt_pk_fp8_f32 v167, v132, v157
	v_mul_f32_e32 v168, s58, v92
	v_mul_f32_e32 v132, s58, v96
	v_med3_f32 v157, v168, s54, v155
	v_med3_f32 v132, v132, s54, v155
	v_cvt_pk_fp8_f32 v167, v157, v132 op_sel:[0,0,1]
	v_mul_f32_e32 v132, s58, v100
	v_mul_f32_e32 v157, s58, v104
	v_med3_f32 v132, v132, s54, v155
	v_med3_f32 v157, v157, s54, v155
	v_mov_b32_e32 v168, v133
	v_cvt_pk_fp8_f32 v168, v132, v157
	v_mul_f32_e32 v169, s58, v108
	v_mul_f32_e32 v132, s58, v112
	v_med3_f32 v157, v169, s54, v155
	v_med3_f32 v132, v132, s54, v155
	v_cvt_pk_fp8_f32 v168, v157, v132 op_sel:[0,0,1]
	v_mul_f32_e32 v132, s58, v116
	v_mul_f32_e32 v157, s58, v120
	v_med3_f32 v132, v132, s54, v155
	v_med3_f32 v157, v157, s54, v155
	v_mov_b32_e32 v169, v133
	v_cvt_pk_fp8_f32 v169, v132, v157
	v_mul_f32_e32 v170, s58, v124
	v_mul_f32_e32 v132, s58, v128
	v_med3_f32 v157, v170, s54, v155
	v_med3_f32 v132, v132, s54, v155
	v_cvt_pk_fp8_f32 v169, v157, v132 op_sel:[0,0,1]
	v_mul_f32_e32 v132, s58, v69
	v_mul_f32_e32 v157, s58, v73
	v_med3_f32 v132, v132, s54, v155
	v_med3_f32 v157, v157, s54, v155
	v_mov_b32_e32 v170, v133
	v_cvt_pk_fp8_f32 v170, v132, v157
	v_mul_f32_e32 v171, s58, v77
	v_mul_f32_e32 v132, s58, v81
	v_med3_f32 v157, v171, s54, v155
	v_med3_f32 v132, v132, s54, v155
	v_cvt_pk_fp8_f32 v170, v157, v132 op_sel:[0,0,1]
	v_mul_f32_e32 v132, s58, v85
	v_mul_f32_e32 v157, s58, v89
	v_med3_f32 v132, v132, s54, v155
	v_med3_f32 v157, v157, s54, v155
	v_mov_b32_e32 v171, v133
	v_cvt_pk_fp8_f32 v171, v132, v157
	v_mul_f32_e32 v172, s58, v93
	v_mul_f32_e32 v132, s58, v97
	v_med3_f32 v157, v172, s54, v155
	v_med3_f32 v132, v132, s54, v155
	v_cvt_pk_fp8_f32 v171, v157, v132 op_sel:[0,0,1]
	v_mul_f32_e32 v132, s58, v101
	v_mul_f32_e32 v157, s58, v105
	v_med3_f32 v132, v132, s54, v155
	v_med3_f32 v157, v157, s54, v155
	v_mov_b32_e32 v172, v133
	v_cvt_pk_fp8_f32 v172, v132, v157
	v_mul_f32_e32 v173, s58, v109
	v_mul_f32_e32 v132, s58, v113
	v_med3_f32 v157, v173, s54, v155
	v_med3_f32 v132, v132, s54, v155
	v_cvt_pk_fp8_f32 v172, v157, v132 op_sel:[0,0,1]
	v_mul_f32_e32 v132, s58, v117
	v_mul_f32_e32 v157, s58, v121
	v_med3_f32 v132, v132, s54, v155
	v_med3_f32 v157, v157, s54, v155
	v_mov_b32_e32 v173, v133
	v_cvt_pk_fp8_f32 v173, v132, v157
	v_mul_f32_e32 v174, s58, v125
	v_mul_f32_e32 v132, s58, v129
	v_med3_f32 v157, v174, s54, v155
	v_med3_f32 v132, v132, s54, v155
	v_cvt_pk_fp8_f32 v173, v157, v132 op_sel:[0,0,1]
	ds_write_b128 v141, v[158:161]
	ds_write_b128 v141, v[162:165] offset:128
	ds_write_b128 v141, v[166:169] offset:256
	ds_write_b128 v141, v[170:173] offset:384
	s_waitcnt lgkmcnt(0)
	ds_read_b128 v[158:161], v143
	ds_read_b128 v[162:165], v145
	v_lshl_add_u64 v[166:167], s[0:1], 0, v[134:135]
	v_mad_i64_i32 v[168:169], s[0:1], s25, v136, v[166:167]
	s_waitcnt lgkmcnt(1)
	global_store_dwordx4 v[168:169], v[158:161], off nt
	v_mad_i64_i32 v[168:169], s[0:1], s25, v138, v[166:167]
	ds_read_b128 v[158:161], v147
	s_waitcnt lgkmcnt(1)
	global_store_dwordx4 v[168:169], v[162:165], off nt
	ds_read_b128 v[162:165], v149
	v_mad_i64_i32 v[168:169], s[0:1], s25, v140, v[166:167]
	s_waitcnt lgkmcnt(1)
	global_store_dwordx4 v[168:169], v[158:161], off nt
	v_mad_i64_i32 v[168:169], s[0:1], s25, v142, v[166:167]
	ds_read_b128 v[158:161], v151
	s_waitcnt lgkmcnt(1)
	global_store_dwordx4 v[168:169], v[162:165], off nt
	ds_read_b128 v[162:165], v152
	v_mad_i64_i32 v[168:169], s[0:1], s25, v144, v[166:167]
	s_waitcnt lgkmcnt(1)
	global_store_dwordx4 v[168:169], v[158:161], off nt
	v_mad_i64_i32 v[168:169], s[0:1], s25, v146, v[166:167]
	ds_read_b128 v[158:161], v153
	s_waitcnt lgkmcnt(1)
	global_store_dwordx4 v[168:169], v[162:165], off nt
	ds_read_b128 v[162:165], v154
	v_mad_i64_i32 v[168:169], s[0:1], s25, v148, v[166:167]
	s_waitcnt lgkmcnt(1)
	global_store_dwordx4 v[168:169], v[158:161], off nt
	s_nop 1
	v_mad_i64_i32 v[158:159], s[0:1], s25, v150, v[166:167]
	s_waitcnt lgkmcnt(0)
	global_store_dwordx4 v[158:159], v[162:165], off nt
	s_waitcnt lgkmcnt(0)
	s_branch .LBB0_238

.LBB0_387:
	v_mul_hi_i32_i24_e32 v3, s14, v132
	v_mul_i32_i24_e32 v2, s14, v132
	v_lshl_add_u64 v[2:3], v[2:3], 2, s[12:13]
	v_lshl_add_u64 v[2:3], v[130:131], 2, v[2:3]
	s_lshl_b64 s[12:13], s[14:15], 2
	v_lshl_add_u64 v[10:11], v[2:3], 0, s[12:13]
	global_load_dwordx4 v[2:5], v[2:3], off nt
	s_nop 0
	global_load_dwordx4 v[6:9], v[10:11], off nt
	v_lshl_add_u64 v[10:11], v[10:11], 0, s[12:13]
	v_lshl_add_u64 v[18:19], v[10:11], 0, s[12:13]
	global_load_dwordx4 v[10:13], v[10:11], off nt
	s_nop 0
	global_load_dwordx4 v[14:17], v[18:19], off nt
	v_lshl_add_u64 v[18:19], v[18:19], 0, s[12:13]
	v_lshl_add_u64 v[26:27], v[18:19], 0, s[12:13]
	global_load_dwordx4 v[18:21], v[18:19], off nt
	s_nop 0
	global_load_dwordx4 v[22:25], v[26:27], off nt
	v_lshl_add_u64 v[26:27], v[26:27], 0, s[12:13]
	v_lshl_add_u64 v[28:29], v[26:27], 0, s[12:13]
	global_load_dwordx4 v[34:37], v[26:27], off nt
	global_load_dwordx4 v[42:45], v[28:29], off nt
	v_lshl_add_u64 v[26:27], v[28:29], 0, s[12:13]
	v_lshl_add_u64 v[38:39], v[26:27], 0, s[12:13]
	v_lshl_add_u64 v[46:47], v[38:39], 0, s[12:13]
	v_lshl_add_u64 v[50:51], v[46:47], 0, s[12:13]
	v_lshl_add_u64 v[54:55], v[50:51], 0, s[12:13]
	v_lshl_add_u64 v[58:59], v[54:55], 0, s[12:13]
	v_lshl_add_u64 v[62:63], v[58:59], 0, s[12:13]
	global_load_dwordx4 v[30:33], v[26:27], off nt
	s_nop 0
	global_load_dwordx4 v[26:29], v[38:39], off nt
	s_nop 0
	global_load_dwordx4 v[38:41], v[46:47], off nt
	s_nop 0
	global_load_dwordx4 v[46:49], v[50:51], off nt
	s_nop 0
	global_load_dwordx4 v[50:53], v[54:55], off nt
	s_nop 0
	global_load_dwordx4 v[54:57], v[58:59], off nt
	s_nop 0
	global_load_dwordx4 v[58:61], v[62:63], off nt
	v_lshl_add_u64 v[62:63], v[62:63], 0, s[12:13]
	global_load_dwordx4 v[62:65], v[62:63], off nt
	s_branch .Lconv_fast_3

.Lconv_fast_3:
	s_andn2_b64 vcc, exec, s[8:9]
	s_cbranch_vccnz .LBB0_333
	s_waitcnt vmcnt(31)
	v_mul_f32_e32 v154, s56, v66
	s_waitcnt vmcnt(30)
	v_mul_f32_e32 v155, s56, v70
	v_med3_f32 v154, v154, s54, v153
	v_med3_f32 v155, v155, s54, v153
	v_mov_b32_e32 v158, 0
	v_cvt_pk_fp8_f32 v158, v154, v155
	s_waitcnt vmcnt(29)
	v_mul_f32_e32 v157, s56, v74
	s_waitcnt vmcnt(28)
	v_mul_f32_e32 v154, s56, v78
	v_med3_f32 v155, v157, s54, v153
	v_med3_f32 v154, v154, s54, v153
	v_cvt_pk_fp8_f32 v158, v155, v154 op_sel:[0,0,1]
	s_waitcnt vmcnt(27)
	v_mul_f32_e32 v154, s56, v82
	s_waitcnt vmcnt(26)
	v_mul_f32_e32 v155, s56, v86
	v_med3_f32 v154, v154, s54, v153
	v_med3_f32 v155, v155, s54, v153
	v_mov_b32_e32 v159, 0
	v_cvt_pk_fp8_f32 v159, v154, v155
	s_waitcnt vmcnt(25)
	v_mul_f32_e32 v157, s56, v90
	s_waitcnt vmcnt(24)
	v_mul_f32_e32 v154, s56, v94
	v_med3_f32 v155, v157, s54, v153
	v_med3_f32 v154, v154, s54, v153
	v_cvt_pk_fp8_f32 v159, v155, v154 op_sel:[0,0,1]
	s_waitcnt vmcnt(23)
	v_mul_f32_e32 v154, s56, v98
	s_waitcnt vmcnt(22)
	v_mul_f32_e32 v155, s56, v102
	v_med3_f32 v154, v154, s54, v153
	v_med3_f32 v155, v155, s54, v153
	v_mov_b32_e32 v160, 0
	v_cvt_pk_fp8_f32 v160, v154, v155
	s_waitcnt vmcnt(21)
	v_mul_f32_e32 v157, s56, v106
	s_waitcnt vmcnt(20)
	v_mul_f32_e32 v154, s56, v110
	v_med3_f32 v155, v157, s54, v153
	v_med3_f32 v154, v154, s54, v153
	v_cvt_pk_fp8_f32 v160, v155, v154 op_sel:[0,0,1]
	s_waitcnt vmcnt(19)
	v_mul_f32_e32 v154, s56, v114
	s_waitcnt vmcnt(18)
	v_mul_f32_e32 v155, s56, v118
	v_med3_f32 v154, v154, s54, v153
	v_med3_f32 v155, v155, s54, v153
	v_mov_b32_e32 v161, 0
	v_cvt_pk_fp8_f32 v161, v154, v155
	s_waitcnt vmcnt(17)
	v_mul_f32_e32 v157, s56, v122
	s_waitcnt vmcnt(16)
	v_mul_f32_e32 v154, s56, v126
	v_med3_f32 v155, v157, s54, v153
	v_med3_f32 v154, v154, s54, v153
	v_cvt_pk_fp8_f32 v161, v155, v154 op_sel:[0,0,1]
	v_mul_f32_e32 v154, s56, v67
	v_mul_f32_e32 v155, s56, v71
	v_med3_f32 v154, v154, s54, v153
	v_med3_f32 v155, v155, s54, v153
	v_mov_b32_e32 v162, 0
	v_cvt_pk_fp8_f32 v162, v154, v155
	v_mul_f32_e32 v157, s56, v75
	v_mul_f32_e32 v154, s56, v79
	v_med3_f32 v155, v157, s54, v153
	v_med3_f32 v154, v154, s54, v153
	v_cvt_pk_fp8_f32 v162, v155, v154 op_sel:[0,0,1]
	v_mul_f32_e32 v154, s56, v83
	v_mul_f32_e32 v155, s56, v87
	v_med3_f32 v154, v154, s54, v153
	v_med3_f32 v155, v155, s54, v153
	v_mov_b32_e32 v163, 0
	v_cvt_pk_fp8_f32 v163, v154, v155
	v_mul_f32_e32 v157, s56, v91
	v_mul_f32_e32 v154, s56, v95
	v_med3_f32 v155, v157, s54, v153
	v_med3_f32 v154, v154, s54, v153
	v_cvt_pk_fp8_f32 v163, v155, v154 op_sel:[0,0,1]
	v_mul_f32_e32 v154, s56, v99
	v_mul_f32_e32 v155, s56, v103
	v_med3_f32 v154, v154, s54, v153
	v_med3_f32 v155, v155, s54, v153
	v_mov_b32_e32 v164, 0
	v_cvt_pk_fp8_f32 v164, v154, v155
	v_mul_f32_e32 v157, s56, v107
	v_mul_f32_e32 v154, s56, v111
	v_med3_f32 v155, v157, s54, v153
	v_med3_f32 v154, v154, s54, v153
	v_cvt_pk_fp8_f32 v164, v155, v154 op_sel:[0,0,1]
	v_mul_f32_e32 v154, s56, v115
	v_mul_f32_e32 v155, s56, v119
	v_med3_f32 v154, v154, s54, v153
	v_med3_f32 v155, v155, s54, v153
	v_mov_b32_e32 v165, 0
	v_cvt_pk_fp8_f32 v165, v154, v155
	v_mul_f32_e32 v157, s56, v123
	v_mul_f32_e32 v154, s56, v127
	v_med3_f32 v155, v157, s54, v153
	v_med3_f32 v154, v154, s54, v153
	v_cvt_pk_fp8_f32 v165, v155, v154 op_sel:[0,0,1]
	v_mul_f32_e32 v154, s56, v68
	v_mul_f32_e32 v155, s56, v72
	v_med3_f32 v154, v154, s54, v153
	v_med3_f32 v155, v155, s54, v153
	v_mov_b32_e32 v166, 0
	v_cvt_pk_fp8_f32 v166, v154, v155
	v_mul_f32_e32 v157, s56, v76
	v_mul_f32_e32 v154, s56, v80
	v_med3_f32 v155, v157, s54, v153
	v_med3_f32 v154, v154, s54, v153
	v_cvt_pk_fp8_f32 v166, v155, v154 op_sel:[0,0,1]
	v_mul_f32_e32 v154, s56, v84
	v_mul_f32_e32 v155, s56, v88
	v_med3_f32 v154, v154, s54, v153
	v_med3_f32 v155, v155, s54, v153
	v_mov_b32_e32 v167, 0
	v_cvt_pk_fp8_f32 v167, v154, v155
	v_mul_f32_e32 v157, s56, v92
	v_mul_f32_e32 v154, s56, v96
	v_med3_f32 v155, v157, s54, v153
	v_med3_f32 v154, v154, s54, v153
	v_cvt_pk_fp8_f32 v167, v155, v154 op_sel:[0,0,1]
	v_mul_f32_e32 v154, s56, v100
	v_mul_f32_e32 v155, s56, v104
	v_med3_f32 v154, v154, s54, v153
	v_med3_f32 v155, v155, s54, v153
	v_mov_b32_e32 v168, 0
	v_cvt_pk_fp8_f32 v168, v154, v155
	v_mul_f32_e32 v157, s56, v108
	v_mul_f32_e32 v154, s56, v112
	v_med3_f32 v155, v157, s54, v153
	v_med3_f32 v154, v154, s54, v153
	v_cvt_pk_fp8_f32 v168, v155, v154 op_sel:[0,0,1]
	v_mul_f32_e32 v154, s56, v116
	v_mul_f32_e32 v155, s56, v120
	v_med3_f32 v154, v154, s54, v153
	v_med3_f32 v155, v155, s54, v153
	v_mov_b32_e32 v169, 0
	v_cvt_pk_fp8_f32 v169, v154, v155
	v_mul_f32_e32 v157, s56, v124
	v_mul_f32_e32 v154, s56, v128
	v_med3_f32 v155, v157, s54, v153
	v_med3_f32 v154, v154, s54, v153
	v_cvt_pk_fp8_f32 v169, v155, v154 op_sel:[0,0,1]
	v_mul_f32_e32 v154, s56, v69
	v_mul_f32_e32 v155, s56, v73
	v_med3_f32 v154, v154, s54, v153
	v_med3_f32 v155, v155, s54, v153
	v_mov_b32_e32 v170, 0
	v_cvt_pk_fp8_f32 v170, v154, v155
	v_mul_f32_e32 v157, s56, v77
	v_mul_f32_e32 v154, s56, v81
	v_med3_f32 v155, v157, s54, v153
	v_med3_f32 v154, v154, s54, v153
	v_cvt_pk_fp8_f32 v170, v155, v154 op_sel:[0,0,1]
	v_mul_f32_e32 v154, s56, v85
	v_mul_f32_e32 v155, s56, v89
	v_med3_f32 v154, v154, s54, v153
	v_med3_f32 v155, v155, s54, v153
	v_mov_b32_e32 v171, 0
	v_cvt_pk_fp8_f32 v171, v154, v155
	v_mul_f32_e32 v157, s56, v93
	v_mul_f32_e32 v154, s56, v97
	v_med3_f32 v155, v157, s54, v153
	v_med3_f32 v154, v154, s54, v153
	v_cvt_pk_fp8_f32 v171, v155, v154 op_sel:[0,0,1]
	v_mul_f32_e32 v154, s56, v101
	v_mul_f32_e32 v155, s56, v105
	v_med3_f32 v154, v154, s54, v153
	v_med3_f32 v155, v155, s54, v153
	v_mov_b32_e32 v172, 0
	v_cvt_pk_fp8_f32 v172, v154, v155
	v_mul_f32_e32 v157, s56, v109
	v_mul_f32_e32 v154, s56, v113
	v_med3_f32 v155, v157, s54, v153
	v_med3_f32 v154, v154, s54, v153
	v_cvt_pk_fp8_f32 v172, v155, v154 op_sel:[0,0,1]
	v_mul_f32_e32 v154, s56, v117
	v_mul_f32_e32 v155, s56, v121
	v_med3_f32 v154, v154, s54, v153
	v_med3_f32 v155, v155, s54, v153
	v_mov_b32_e32 v173, 0
	v_cvt_pk_fp8_f32 v173, v154, v155
	v_mul_f32_e32 v157, s56, v125
	v_mul_f32_e32 v154, s56, v129
	v_med3_f32 v155, v157, s54, v153
	v_med3_f32 v154, v154, s54, v153
	v_cvt_pk_fp8_f32 v173, v155, v154 op_sel:[0,0,1]
	ds_write_b128 v137, v[158:161]
	ds_write_b128 v137, v[162:165] offset:128
	ds_write_b128 v137, v[166:169] offset:256
	ds_write_b128 v137, v[170:173] offset:384
	s_waitcnt lgkmcnt(0)
	ds_read_b128 v[158:161], v139
	ds_read_b128 v[162:165], v141
	v_lshl_add_u64 v[154:155], s[0:1], 0, v[134:135]
	v_mad_i64_i32 v[166:167], s[0:1], s24, v136, v[154:155]
	s_waitcnt lgkmcnt(1)
	global_store_dwordx4 v[166:167], v[158:161], off nt
	v_mad_i64_i32 v[166:167], s[0:1], s24, v138, v[154:155]
	ds_read_b128 v[158:161], v143
	s_waitcnt lgkmcnt(1)
	global_store_dwordx4 v[166:167], v[162:165], off nt
	ds_read_b128 v[162:165], v145
	v_mad_i64_i32 v[166:167], s[0:1], s24, v140, v[154:155]
	s_waitcnt lgkmcnt(1)
	global_store_dwordx4 v[166:167], v[158:161], off nt
	v_mad_i64_i32 v[166:167], s[0:1], s24, v142, v[154:155]
	ds_read_b128 v[158:161], v147
	s_waitcnt lgkmcnt(1)
	global_store_dwordx4 v[166:167], v[162:165], off nt
	ds_read_b128 v[162:165], v149
	v_mad_i64_i32 v[166:167], s[0:1], s24, v144, v[154:155]
	s_waitcnt lgkmcnt(1)
	global_store_dwordx4 v[166:167], v[158:161], off nt
	v_mad_i64_i32 v[166:167], s[0:1], s24, v146, v[154:155]
	ds_read_b128 v[158:161], v151
	s_waitcnt lgkmcnt(1)
	global_store_dwordx4 v[166:167], v[162:165], off nt
	ds_read_b128 v[162:165], v152
	v_mad_i64_i32 v[166:167], s[0:1], s24, v148, v[154:155]
	v_mad_i64_i32 v[154:155], s[0:1], s24, v150, v[154:155]
	s_waitcnt lgkmcnt(1)
	global_store_dwordx4 v[166:167], v[158:161], off nt
	s_waitcnt lgkmcnt(0)
	global_store_dwordx4 v[154:155], v[162:165], off nt
	s_waitcnt lgkmcnt(0)
	s_branch .LBB0_333

.LBB0_699:
	s_cmp_ge_u32 s53, 4
	s_cselect_b32 s36, 1, 0
	s_cmp_ge_u32 s53, 5
	s_cselect_b32 s53, 1, 0
	s_add_i32 s36, s36, s53
	v_readlane_b32 s84, v253, 22
	s_cmp_lg_u32 s36, 1
	v_readlane_b32 s85, v253, 23
	v_readlane_b32 s86, v253, 24
	v_readlane_b32 s87, v253, 25
	v_readlane_b32 s88, v253, 26
	v_readlane_b32 s89, v253, 27
	v_readlane_b32 s90, v253, 28
	v_readlane_b32 s91, v253, 29
	s_cbranch_scc1 .LBB0_1060
	s_lshl_b32 s22, s96, 3
	s_abs_i32 s20, s22
	v_cvt_f32_u32_e32 v2, s20
	s_sub_i32 s0, 0, s20
	s_add_i32 s16, s22, s50
	s_lshl_b32 s25, s97, 3
	v_rcp_iflag_f32_e32 v2, v2
	s_add_i32 s16, s16, -1
	s_add_i32 s26, s25, s94
	s_abs_i32 s14, s16
	v_mul_f32_e32 v2, 0x4f7ffffe, v2
	v_cvt_u32_f32_e32 v2, v2
	s_waitcnt vmcnt(0) lgkmcnt(0)
	s_barrier
	v_readfirstlane_b32 s21, v2
	s_mul_i32 s0, s0, s21
	s_mul_hi_u32 s0, s21, s0
	s_add_i32 s21, s21, s0
	s_cmp_ge_i32 s26, s50
	s_mul_hi_u32 s15, s14, s21
	s_cbranch_scc1 .LBB0_708
	s_add_i32 s17, s26, 0xcc0
	s_cmpk_gt_i32 s26, 0xf7ff
	s_cbranch_scc0 .LBB0_709
	s_cmpk_gt_u32 s17, 0x5bf
	s_cbranch_scc0 .LBB0_710
	s_cmpk_gt_u32 s17, 0x6bf
	s_cbranch_scc0 .LBB0_711
	s_cmpk_gt_u32 s17, 0x8bf
	s_cbranch_scc0 .LBB0_712
	s_cmp_lt_u32 s26, 0xfffff340
	s_cbranch_scc0 .LBB0_713
	s_mul_hi_u32 s0, s26, 0xaaaaaaab
	s_lshr_b32 s10, s0, 8
	s_mul_i32 s18, s10, 0xfffffe80
	s_add_i32 s18, s18, s26
	s_cmpk_gt_i32 s18, 0xff
	s_cbranch_scc0 .LBB0_714
	s_add_i32 s0, s18, 0xffffff00
	s_lshr_b32 s0, s0, 4
	s_lshl_b32 s12, s10, 20
	s_mov_b32 s13, 0
	v_readlane_b32 s56, v253, 31
	s_and_b32 s0, s0, 0xffffffe
	s_lshl_b64 s[2:3], s[12:13], 2
	v_readlane_b32 s66, v253, 41
	v_readlane_b32 s67, v253, 42
	s_add_u32 s1, s66, s2
	s_addc_u32 s2, s67, s3
	s_cmpk_lt_u32 s26, 0x6000
	s_cselect_b32 s12, s1, s84
	s_mov_b32 s1, s13
	s_cselect_b32 s11, s2, s85
	s_lshl_b64 s[2:3], s[0:1], 19
	s_add_u32 s1, s12, s2
	s_addc_u32 s3, s11, s3
	s_lshl_b32 s2, s26, 6
	s_and_b32 s19, s2, 0x7c0
	s_lshl_b32 s2, s19, 2
	s_add_u32 s2, s1, s2
	s_mov_b32 s11, s13
	s_addc_u32 s3, s3, 0
	s_lshl_b64 s[12:13], s[10:11], 20
	s_lshl_b32 s1, s19, 9
	s_add_u32 s11, s90, s12
	s_addc_u32 s12, s91, s13
	s_add_u32 s1, s11, s1
	s_addc_u32 s11, s12, 0
	s_lshl_b32 s0, s0, 6
	s_add_u32 s0, s1, s0
	s_addc_u32 s1, s11, 0
	s_add_u32 s0, s0, 0x30c00000
	v_readlane_b32 s57, v253, 32
	v_readlane_b32 s58, v253, 33
	v_readlane_b32 s59, v253, 34
	v_readlane_b32 s60, v253, 35
	v_readlane_b32 s61, v253, 36
	v_readlane_b32 s62, v253, 37
	v_readlane_b32 s63, v253, 38
	v_readlane_b32 s64, v253, 39
	v_readlane_b32 s65, v253, 40
	v_readlane_b32 s68, v253, 43
	v_readlane_b32 s69, v253, 44
	v_readlane_b32 s70, v253, 45
	v_readlane_b32 s71, v253, 46
	s_addc_u32 s1, s1, 0
	s_mov_b64 s[12:13], 0
	s_branch .LBB0_715

.LBB0_789:
	v_mul_u32_u24_e32 v2, s16, v131
	v_lshlrev_b32_e32 v132, 2, v2
	v_lshl_add_u64 v[2:3], s[14:15], 0, v[132:133]
	v_lshlrev_b32_e32 v132, 2, v130
	v_lshl_add_u64 v[2:3], v[2:3], 0, v[132:133]
	s_lshl_b64 s[14:15], s[16:17], 2
	v_lshl_add_u64 v[10:11], v[2:3], 0, s[14:15]
	global_load_dwordx4 v[2:5], v[2:3], off nt
	s_nop 0
	global_load_dwordx4 v[6:9], v[10:11], off nt
	v_lshl_add_u64 v[10:11], v[10:11], 0, s[14:15]
	v_lshl_add_u64 v[18:19], v[10:11], 0, s[14:15]
	global_load_dwordx4 v[10:13], v[10:11], off nt
	s_nop 0
	global_load_dwordx4 v[14:17], v[18:19], off nt
	v_lshl_add_u64 v[18:19], v[18:19], 0, s[14:15]
	v_lshl_add_u64 v[26:27], v[18:19], 0, s[14:15]
	global_load_dwordx4 v[18:21], v[18:19], off nt
	s_nop 0
	global_load_dwordx4 v[22:25], v[26:27], off nt
	v_lshl_add_u64 v[26:27], v[26:27], 0, s[14:15]
	v_lshl_add_u64 v[28:29], v[26:27], 0, s[14:15]
	global_load_dwordx4 v[34:37], v[26:27], off nt
	global_load_dwordx4 v[42:45], v[28:29], off nt
	v_lshl_add_u64 v[26:27], v[28:29], 0, s[14:15]
	v_lshl_add_u64 v[38:39], v[26:27], 0, s[14:15]
	v_lshl_add_u64 v[46:47], v[38:39], 0, s[14:15]
	v_lshl_add_u64 v[50:51], v[46:47], 0, s[14:15]
	v_lshl_add_u64 v[54:55], v[50:51], 0, s[14:15]
	v_lshl_add_u64 v[58:59], v[54:55], 0, s[14:15]
	v_lshl_add_u64 v[62:63], v[58:59], 0, s[14:15]
	global_load_dwordx4 v[30:33], v[26:27], off nt
	s_nop 0
	global_load_dwordx4 v[26:29], v[38:39], off nt
	s_nop 0
	global_load_dwordx4 v[38:41], v[46:47], off nt
	s_nop 0
	global_load_dwordx4 v[46:49], v[50:51], off nt
	s_nop 0
	global_load_dwordx4 v[50:53], v[54:55], off nt
	s_nop 0
	global_load_dwordx4 v[54:57], v[58:59], off nt
	s_nop 0
	global_load_dwordx4 v[58:61], v[62:63], off nt
	v_lshl_add_u64 v[62:63], v[62:63], 0, s[14:15]
	global_load_dwordx4 v[62:65], v[62:63], off nt
	s_branch .Lconv_fast_1

.Lconv_fast_1:
	s_andn2_b64 vcc, exec, s[10:11]
	s_cbranch_vccnz .LBB0_735
	s_waitcnt vmcnt(31)
	v_mul_f32_e32 v132, s60, v66
	s_waitcnt vmcnt(30)
	v_mul_f32_e32 v157, s60, v70
	v_med3_f32 v132, v132, s56, v155
	v_med3_f32 v157, v157, s56, v155
	v_mov_b32_e32 v158, v133
	v_cvt_pk_fp8_f32 v158, v132, v157
	s_waitcnt vmcnt(29)
	v_mul_f32_e32 v159, s60, v74
	s_waitcnt vmcnt(28)
	v_mul_f32_e32 v132, s60, v78
	v_med3_f32 v157, v159, s56, v155
	v_med3_f32 v132, v132, s56, v155
	v_cvt_pk_fp8_f32 v158, v157, v132 op_sel:[0,0,1]
	s_waitcnt vmcnt(27)
	v_mul_f32_e32 v132, s60, v82
	s_waitcnt vmcnt(26)
	v_mul_f32_e32 v157, s60, v86
	v_med3_f32 v132, v132, s56, v155
	v_med3_f32 v157, v157, s56, v155
	v_mov_b32_e32 v159, v133
	v_cvt_pk_fp8_f32 v159, v132, v157
	s_waitcnt vmcnt(25)
	v_mul_f32_e32 v160, s60, v90
	s_waitcnt vmcnt(24)
	v_mul_f32_e32 v132, s60, v94
	v_med3_f32 v157, v160, s56, v155
	v_med3_f32 v132, v132, s56, v155
	v_cvt_pk_fp8_f32 v159, v157, v132 op_sel:[0,0,1]
	s_waitcnt vmcnt(23)
	v_mul_f32_e32 v132, s60, v98
	s_waitcnt vmcnt(22)
	v_mul_f32_e32 v157, s60, v102
	v_med3_f32 v132, v132, s56, v155
	v_med3_f32 v157, v157, s56, v155
	v_mov_b32_e32 v160, v133
	v_cvt_pk_fp8_f32 v160, v132, v157
	s_waitcnt vmcnt(21)
	v_mul_f32_e32 v161, s60, v106
	s_waitcnt vmcnt(20)
	v_mul_f32_e32 v132, s60, v110
	v_med3_f32 v157, v161, s56, v155
	v_med3_f32 v132, v132, s56, v155
	v_cvt_pk_fp8_f32 v160, v157, v132 op_sel:[0,0,1]
	s_waitcnt vmcnt(19)
	v_mul_f32_e32 v132, s60, v114
	s_waitcnt vmcnt(18)
	v_mul_f32_e32 v157, s60, v118
	v_med3_f32 v132, v132, s56, v155
	v_med3_f32 v157, v157, s56, v155
	v_mov_b32_e32 v161, v133
	v_cvt_pk_fp8_f32 v161, v132, v157
	s_waitcnt vmcnt(17)
	v_mul_f32_e32 v162, s60, v122
	s_waitcnt vmcnt(16)
	v_mul_f32_e32 v132, s60, v126
	v_med3_f32 v157, v162, s56, v155
	v_med3_f32 v132, v132, s56, v155
	v_cvt_pk_fp8_f32 v161, v157, v132 op_sel:[0,0,1]
	v_mul_f32_e32 v132, s60, v67
	v_mul_f32_e32 v157, s60, v71
	v_med3_f32 v132, v132, s56, v155
	v_med3_f32 v157, v157, s56, v155
	v_mov_b32_e32 v162, v133
	v_cvt_pk_fp8_f32 v162, v132, v157
	v_mul_f32_e32 v163, s60, v75
	v_mul_f32_e32 v132, s60, v79
	v_med3_f32 v157, v163, s56, v155
	v_med3_f32 v132, v132, s56, v155
	v_cvt_pk_fp8_f32 v162, v157, v132 op_sel:[0,0,1]
	v_mul_f32_e32 v132, s60, v83
	v_mul_f32_e32 v157, s60, v87
	v_med3_f32 v132, v132, s56, v155
	v_med3_f32 v157, v157, s56, v155
	v_mov_b32_e32 v163, v133
	v_cvt_pk_fp8_f32 v163, v132, v157
	v_mul_f32_e32 v164, s60, v91
	v_mul_f32_e32 v132, s60, v95
	v_med3_f32 v157, v164, s56, v155
	v_med3_f32 v132, v132, s56, v155
	v_cvt_pk_fp8_f32 v163, v157, v132 op_sel:[0,0,1]
	v_mul_f32_e32 v132, s60, v99
	v_mul_f32_e32 v157, s60, v103
	v_med3_f32 v132, v132, s56, v155
	v_med3_f32 v157, v157, s56, v155
	v_mov_b32_e32 v164, v133
	v_cvt_pk_fp8_f32 v164, v132, v157
	v_mul_f32_e32 v165, s60, v107
	v_mul_f32_e32 v132, s60, v111
	v_med3_f32 v157, v165, s56, v155
	v_med3_f32 v132, v132, s56, v155
	v_cvt_pk_fp8_f32 v164, v157, v132 op_sel:[0,0,1]
	v_mul_f32_e32 v132, s60, v115
	v_mul_f32_e32 v157, s60, v119
	v_med3_f32 v132, v132, s56, v155
	v_med3_f32 v157, v157, s56, v155
	v_mov_b32_e32 v165, v133
	v_cvt_pk_fp8_f32 v165, v132, v157
	v_mul_f32_e32 v166, s60, v123
	v_mul_f32_e32 v132, s60, v127
	v_med3_f32 v157, v166, s56, v155
	v_med3_f32 v132, v132, s56, v155
	v_cvt_pk_fp8_f32 v165, v157, v132 op_sel:[0,0,1]
	v_mul_f32_e32 v132, s60, v68
	v_mul_f32_e32 v157, s60, v72
	v_med3_f32 v132, v132, s56, v155
	v_med3_f32 v157, v157, s56, v155
	v_mov_b32_e32 v166, v133
	v_cvt_pk_fp8_f32 v166, v132, v157
	v_mul_f32_e32 v167, s60, v76
	v_mul_f32_e32 v132, s60, v80
	v_med3_f32 v157, v167, s56, v155
	v_med3_f32 v132, v132, s56, v155
	v_cvt_pk_fp8_f32 v166, v157, v132 op_sel:[0,0,1]
	v_mul_f32_e32 v132, s60, v84
	v_mul_f32_e32 v157, s60, v88
	v_med3_f32 v132, v132, s56, v155
	v_med3_f32 v157, v157, s56, v155
	v_mov_b32_e32 v167, v133
	v_cvt_pk_fp8_f32 v167, v132, v157
	v_mul_f32_e32 v168, s60, v92
	v_mul_f32_e32 v132, s60, v96
	v_med3_f32 v157, v168, s56, v155
	v_med3_f32 v132, v132, s56, v155
	v_cvt_pk_fp8_f32 v167, v157, v132 op_sel:[0,0,1]
	v_mul_f32_e32 v132, s60, v100
	v_mul_f32_e32 v157, s60, v104
	v_med3_f32 v132, v132, s56, v155
	v_med3_f32 v157, v157, s56, v155
	v_mov_b32_e32 v168, v133
	v_cvt_pk_fp8_f32 v168, v132, v157
	v_mul_f32_e32 v169, s60, v108
	v_mul_f32_e32 v132, s60, v112
	v_med3_f32 v157, v169, s56, v155
	v_med3_f32 v132, v132, s56, v155
	v_cvt_pk_fp8_f32 v168, v157, v132 op_sel:[0,0,1]
	v_mul_f32_e32 v132, s60, v116
	v_mul_f32_e32 v157, s60, v120
	v_med3_f32 v132, v132, s56, v155
	v_med3_f32 v157, v157, s56, v155
	v_mov_b32_e32 v169, v133
	v_cvt_pk_fp8_f32 v169, v132, v157
	v_mul_f32_e32 v170, s60, v124
	v_mul_f32_e32 v132, s60, v128
	v_med3_f32 v157, v170, s56, v155
	v_med3_f32 v132, v132, s56, v155
	v_cvt_pk_fp8_f32 v169, v157, v132 op_sel:[0,0,1]
	v_mul_f32_e32 v132, s60, v69
	v_mul_f32_e32 v157, s60, v73
	v_med3_f32 v132, v132, s56, v155
	v_med3_f32 v157, v157, s56, v155
	v_mov_b32_e32 v170, v133
	v_cvt_pk_fp8_f32 v170, v132, v157
	v_mul_f32_e32 v171, s60, v77
	v_mul_f32_e32 v132, s60, v81
	v_med3_f32 v157, v171, s56, v155
	v_med3_f32 v132, v132, s56, v155
	v_cvt_pk_fp8_f32 v170, v157, v132 op_sel:[0,0,1]
	v_mul_f32_e32 v132, s60, v85
	v_mul_f32_e32 v157, s60, v89
	v_med3_f32 v132, v132, s56, v155
	v_med3_f32 v157, v157, s56, v155
	v_mov_b32_e32 v171, v133
	v_cvt_pk_fp8_f32 v171, v132, v157
	v_mul_f32_e32 v172, s60, v93
	v_mul_f32_e32 v132, s60, v97
	v_med3_f32 v157, v172, s56, v155
	v_med3_f32 v132, v132, s56, v155
	v_cvt_pk_fp8_f32 v171, v157, v132 op_sel:[0,0,1]
	v_mul_f32_e32 v132, s60, v101
	v_mul_f32_e32 v157, s60, v105
	v_med3_f32 v132, v132, s56, v155
	v_med3_f32 v157, v157, s56, v155
	v_mov_b32_e32 v172, v133
	v_cvt_pk_fp8_f32 v172, v132, v157
	v_mul_f32_e32 v173, s60, v109
	v_mul_f32_e32 v132, s60, v113
	v_med3_f32 v157, v173, s56, v155
	v_med3_f32 v132, v132, s56, v155
	v_cvt_pk_fp8_f32 v172, v157, v132 op_sel:[0,0,1]
	v_mul_f32_e32 v132, s60, v117
	v_mul_f32_e32 v157, s60, v121
	v_med3_f32 v132, v132, s56, v155
	v_med3_f32 v157, v157, s56, v155
	v_mov_b32_e32 v173, v133
	v_cvt_pk_fp8_f32 v173, v132, v157
	v_mul_f32_e32 v174, s60, v125
	v_mul_f32_e32 v132, s60, v129
	v_med3_f32 v157, v174, s56, v155
	v_med3_f32 v132, v132, s56, v155
	v_cvt_pk_fp8_f32 v173, v157, v132 op_sel:[0,0,1]
	ds_write_b128 v141, v[158:161]
	ds_write_b128 v141, v[162:165] offset:128
	ds_write_b128 v141, v[166:169] offset:256
	ds_write_b128 v141, v[170:173] offset:384
	s_waitcnt lgkmcnt(0)
	ds_read_b128 v[158:161], v143
	ds_read_b128 v[162:165], v145
	v_lshl_add_u64 v[166:167], s[0:1], 0, v[134:135]
	v_mad_i64_i32 v[168:169], s[0:1], s27, v136, v[166:167]
	s_waitcnt lgkmcnt(1)
	global_store_dwordx4 v[168:169], v[158:161], off nt
	v_mad_i64_i32 v[168:169], s[0:1], s27, v138, v[166:167]
	ds_read_b128 v[158:161], v147
	s_waitcnt lgkmcnt(1)
	global_store_dwordx4 v[168:169], v[162:165], off nt
	ds_read_b128 v[162:165], v149
	v_mad_i64_i32 v[168:169], s[0:1], s27, v140, v[166:167]
	s_waitcnt lgkmcnt(1)
	global_store_dwordx4 v[168:169], v[158:161], off nt
	v_mad_i64_i32 v[168:169], s[0:1], s27, v142, v[166:167]
	ds_read_b128 v[158:161], v151
	s_waitcnt lgkmcnt(1)
	global_store_dwordx4 v[168:169], v[162:165], off nt
	ds_read_b128 v[162:165], v152
	v_mad_i64_i32 v[168:169], s[0:1], s27, v144, v[166:167]
	s_waitcnt lgkmcnt(1)
	global_store_dwordx4 v[168:169], v[158:161], off nt
	v_mad_i64_i32 v[168:169], s[0:1], s27, v146, v[166:167]
	ds_read_b128 v[158:161], v153
	s_waitcnt lgkmcnt(1)
	global_store_dwordx4 v[168:169], v[162:165], off nt
	ds_read_b128 v[162:165], v154
	v_mad_i64_i32 v[168:169], s[0:1], s27, v148, v[166:167]
	s_waitcnt lgkmcnt(1)
	global_store_dwordx4 v[168:169], v[158:161], off nt
	s_nop 1
	v_mad_i64_i32 v[158:159], s[0:1], s27, v150, v[166:167]
	s_waitcnt lgkmcnt(0)
	global_store_dwordx4 v[158:159], v[162:165], off nt
	s_waitcnt lgkmcnt(0)
	s_branch .LBB0_735

.LBB0_884:
	v_mul_hi_i32_i24_e32 v3, s16, v132
	v_mul_i32_i24_e32 v2, s16, v132
	v_lshl_add_u64 v[2:3], v[2:3], 2, s[14:15]
	v_lshl_add_u64 v[2:3], v[130:131], 2, v[2:3]
	s_lshl_b64 s[14:15], s[16:17], 2
	v_lshl_add_u64 v[10:11], v[2:3], 0, s[14:15]
	global_load_dwordx4 v[2:5], v[2:3], off nt
	s_nop 0
	global_load_dwordx4 v[6:9], v[10:11], off nt
	v_lshl_add_u64 v[10:11], v[10:11], 0, s[14:15]
	v_lshl_add_u64 v[18:19], v[10:11], 0, s[14:15]
	global_load_dwordx4 v[10:13], v[10:11], off nt
	s_nop 0
	global_load_dwordx4 v[14:17], v[18:19], off nt
	v_lshl_add_u64 v[18:19], v[18:19], 0, s[14:15]
	v_lshl_add_u64 v[26:27], v[18:19], 0, s[14:15]
	global_load_dwordx4 v[18:21], v[18:19], off nt
	s_nop 0
	global_load_dwordx4 v[22:25], v[26:27], off nt
	v_lshl_add_u64 v[26:27], v[26:27], 0, s[14:15]
	v_lshl_add_u64 v[28:29], v[26:27], 0, s[14:15]
	global_load_dwordx4 v[34:37], v[26:27], off nt
	global_load_dwordx4 v[42:45], v[28:29], off nt
	v_lshl_add_u64 v[26:27], v[28:29], 0, s[14:15]
	v_lshl_add_u64 v[38:39], v[26:27], 0, s[14:15]
	v_lshl_add_u64 v[46:47], v[38:39], 0, s[14:15]
	v_lshl_add_u64 v[50:51], v[46:47], 0, s[14:15]
	v_lshl_add_u64 v[54:55], v[50:51], 0, s[14:15]
	v_lshl_add_u64 v[58:59], v[54:55], 0, s[14:15]
	v_lshl_add_u64 v[62:63], v[58:59], 0, s[14:15]
	global_load_dwordx4 v[30:33], v[26:27], off nt
	s_nop 0
	global_load_dwordx4 v[26:29], v[38:39], off nt
	s_nop 0
	global_load_dwordx4 v[38:41], v[46:47], off nt
	s_nop 0
	global_load_dwordx4 v[46:49], v[50:51], off nt
	s_nop 0
	global_load_dwordx4 v[50:53], v[54:55], off nt
	s_nop 0
	global_load_dwordx4 v[54:57], v[58:59], off nt
	s_nop 0
	global_load_dwordx4 v[58:61], v[62:63], off nt
	v_lshl_add_u64 v[62:63], v[62:63], 0, s[14:15]
	global_load_dwordx4 v[62:65], v[62:63], off nt
	s_branch .Lconv_fast_4

.Lconv_fast_4:
	s_andn2_b64 vcc, exec, s[10:11]
	s_cbranch_vccnz .LBB0_830
	s_waitcnt vmcnt(31)
	v_mul_f32_e32 v154, s58, v66
	s_waitcnt vmcnt(30)
	v_mul_f32_e32 v155, s58, v70
	v_med3_f32 v154, v154, s56, v153
	v_med3_f32 v155, v155, s56, v153
	v_mov_b32_e32 v158, 0
	v_cvt_pk_fp8_f32 v158, v154, v155
	s_waitcnt vmcnt(29)
	v_mul_f32_e32 v157, s58, v74
	s_waitcnt vmcnt(28)
	v_mul_f32_e32 v154, s58, v78
	v_med3_f32 v155, v157, s56, v153
	v_med3_f32 v154, v154, s56, v153
	v_cvt_pk_fp8_f32 v158, v155, v154 op_sel:[0,0,1]
	s_waitcnt vmcnt(27)
	v_mul_f32_e32 v154, s58, v82
	s_waitcnt vmcnt(26)
	v_mul_f32_e32 v155, s58, v86
	v_med3_f32 v154, v154, s56, v153
	v_med3_f32 v155, v155, s56, v153
	v_mov_b32_e32 v159, 0
	v_cvt_pk_fp8_f32 v159, v154, v155
	s_waitcnt vmcnt(25)
	v_mul_f32_e32 v157, s58, v90
	s_waitcnt vmcnt(24)
	v_mul_f32_e32 v154, s58, v94
	v_med3_f32 v155, v157, s56, v153
	v_med3_f32 v154, v154, s56, v153
	v_cvt_pk_fp8_f32 v159, v155, v154 op_sel:[0,0,1]
	s_waitcnt vmcnt(23)
	v_mul_f32_e32 v154, s58, v98
	s_waitcnt vmcnt(22)
	v_mul_f32_e32 v155, s58, v102
	v_med3_f32 v154, v154, s56, v153
	v_med3_f32 v155, v155, s56, v153
	v_mov_b32_e32 v160, 0
	v_cvt_pk_fp8_f32 v160, v154, v155
	s_waitcnt vmcnt(21)
	v_mul_f32_e32 v157, s58, v106
	s_waitcnt vmcnt(20)
	v_mul_f32_e32 v154, s58, v110
	v_med3_f32 v155, v157, s56, v153
	v_med3_f32 v154, v154, s56, v153
	v_cvt_pk_fp8_f32 v160, v155, v154 op_sel:[0,0,1]
	s_waitcnt vmcnt(19)
	v_mul_f32_e32 v154, s58, v114
	s_waitcnt vmcnt(18)
	v_mul_f32_e32 v155, s58, v118
	v_med3_f32 v154, v154, s56, v153
	v_med3_f32 v155, v155, s56, v153
	v_mov_b32_e32 v161, 0
	v_cvt_pk_fp8_f32 v161, v154, v155
	s_waitcnt vmcnt(17)
	v_mul_f32_e32 v157, s58, v122
	s_waitcnt vmcnt(16)
	v_mul_f32_e32 v154, s58, v126
	v_med3_f32 v155, v157, s56, v153
	v_med3_f32 v154, v154, s56, v153
	v_cvt_pk_fp8_f32 v161, v155, v154 op_sel:[0,0,1]
	v_mul_f32_e32 v154, s58, v67
	v_mul_f32_e32 v155, s58, v71
	v_med3_f32 v154, v154, s56, v153
	v_med3_f32 v155, v155, s56, v153
	v_mov_b32_e32 v162, 0
	v_cvt_pk_fp8_f32 v162, v154, v155
	v_mul_f32_e32 v157, s58, v75
	v_mul_f32_e32 v154, s58, v79
	v_med3_f32 v155, v157, s56, v153
	v_med3_f32 v154, v154, s56, v153
	v_cvt_pk_fp8_f32 v162, v155, v154 op_sel:[0,0,1]
	v_mul_f32_e32 v154, s58, v83
	v_mul_f32_e32 v155, s58, v87
	v_med3_f32 v154, v154, s56, v153
	v_med3_f32 v155, v155, s56, v153
	v_mov_b32_e32 v163, 0
	v_cvt_pk_fp8_f32 v163, v154, v155
	v_mul_f32_e32 v157, s58, v91
	v_mul_f32_e32 v154, s58, v95
	v_med3_f32 v155, v157, s56, v153
	v_med3_f32 v154, v154, s56, v153
	v_cvt_pk_fp8_f32 v163, v155, v154 op_sel:[0,0,1]
	v_mul_f32_e32 v154, s58, v99
	v_mul_f32_e32 v155, s58, v103
	v_med3_f32 v154, v154, s56, v153
	v_med3_f32 v155, v155, s56, v153
	v_mov_b32_e32 v164, 0
	v_cvt_pk_fp8_f32 v164, v154, v155
	v_mul_f32_e32 v157, s58, v107
	v_mul_f32_e32 v154, s58, v111
	v_med3_f32 v155, v157, s56, v153
	v_med3_f32 v154, v154, s56, v153
	v_cvt_pk_fp8_f32 v164, v155, v154 op_sel:[0,0,1]
	v_mul_f32_e32 v154, s58, v115
	v_mul_f32_e32 v155, s58, v119
	v_med3_f32 v154, v154, s56, v153
	v_med3_f32 v155, v155, s56, v153
	v_mov_b32_e32 v165, 0
	v_cvt_pk_fp8_f32 v165, v154, v155
	v_mul_f32_e32 v157, s58, v123
	v_mul_f32_e32 v154, s58, v127
	v_med3_f32 v155, v157, s56, v153
	v_med3_f32 v154, v154, s56, v153
	v_cvt_pk_fp8_f32 v165, v155, v154 op_sel:[0,0,1]
	v_mul_f32_e32 v154, s58, v68
	v_mul_f32_e32 v155, s58, v72
	v_med3_f32 v154, v154, s56, v153
	v_med3_f32 v155, v155, s56, v153
	v_mov_b32_e32 v166, 0
	v_cvt_pk_fp8_f32 v166, v154, v155
	v_mul_f32_e32 v157, s58, v76
	v_mul_f32_e32 v154, s58, v80
	v_med3_f32 v155, v157, s56, v153
	v_med3_f32 v154, v154, s56, v153
	v_cvt_pk_fp8_f32 v166, v155, v154 op_sel:[0,0,1]
	v_mul_f32_e32 v154, s58, v84
	v_mul_f32_e32 v155, s58, v88
	v_med3_f32 v154, v154, s56, v153
	v_med3_f32 v155, v155, s56, v153
	v_mov_b32_e32 v167, 0
	v_cvt_pk_fp8_f32 v167, v154, v155
	v_mul_f32_e32 v157, s58, v92
	v_mul_f32_e32 v154, s58, v96
	v_med3_f32 v155, v157, s56, v153
	v_med3_f32 v154, v154, s56, v153
	v_cvt_pk_fp8_f32 v167, v155, v154 op_sel:[0,0,1]
	v_mul_f32_e32 v154, s58, v100
	v_mul_f32_e32 v155, s58, v104
	v_med3_f32 v154, v154, s56, v153
	v_med3_f32 v155, v155, s56, v153
	v_mov_b32_e32 v168, 0
	v_cvt_pk_fp8_f32 v168, v154, v155
	v_mul_f32_e32 v157, s58, v108
	v_mul_f32_e32 v154, s58, v112
	v_med3_f32 v155, v157, s56, v153
	v_med3_f32 v154, v154, s56, v153
	v_cvt_pk_fp8_f32 v168, v155, v154 op_sel:[0,0,1]
	v_mul_f32_e32 v154, s58, v116
	v_mul_f32_e32 v155, s58, v120
	v_med3_f32 v154, v154, s56, v153
	v_med3_f32 v155, v155, s56, v153
	v_mov_b32_e32 v169, 0
	v_cvt_pk_fp8_f32 v169, v154, v155
	v_mul_f32_e32 v157, s58, v124
	v_mul_f32_e32 v154, s58, v128
	v_med3_f32 v155, v157, s56, v153
	v_med3_f32 v154, v154, s56, v153
	v_cvt_pk_fp8_f32 v169, v155, v154 op_sel:[0,0,1]
	v_mul_f32_e32 v154, s58, v69
	v_mul_f32_e32 v155, s58, v73
	v_med3_f32 v154, v154, s56, v153
	v_med3_f32 v155, v155, s56, v153
	v_mov_b32_e32 v170, 0
	v_cvt_pk_fp8_f32 v170, v154, v155
	v_mul_f32_e32 v157, s58, v77
	v_mul_f32_e32 v154, s58, v81
	v_med3_f32 v155, v157, s56, v153
	v_med3_f32 v154, v154, s56, v153
	v_cvt_pk_fp8_f32 v170, v155, v154 op_sel:[0,0,1]
	v_mul_f32_e32 v154, s58, v85
	v_mul_f32_e32 v155, s58, v89
	v_med3_f32 v154, v154, s56, v153
	v_med3_f32 v155, v155, s56, v153
	v_mov_b32_e32 v171, 0
	v_cvt_pk_fp8_f32 v171, v154, v155
	v_mul_f32_e32 v157, s58, v93
	v_mul_f32_e32 v154, s58, v97
	v_med3_f32 v155, v157, s56, v153
	v_med3_f32 v154, v154, s56, v153
	v_cvt_pk_fp8_f32 v171, v155, v154 op_sel:[0,0,1]
	v_mul_f32_e32 v154, s58, v101
	v_mul_f32_e32 v155, s58, v105
	v_med3_f32 v154, v154, s56, v153
	v_med3_f32 v155, v155, s56, v153
	v_mov_b32_e32 v172, 0
	v_cvt_pk_fp8_f32 v172, v154, v155
	v_mul_f32_e32 v157, s58, v109
	v_mul_f32_e32 v154, s58, v113
	v_med3_f32 v155, v157, s56, v153
	v_med3_f32 v154, v154, s56, v153
	v_cvt_pk_fp8_f32 v172, v155, v154 op_sel:[0,0,1]
	v_mul_f32_e32 v154, s58, v117
	v_mul_f32_e32 v155, s58, v121
	v_med3_f32 v154, v154, s56, v153
	v_med3_f32 v155, v155, s56, v153
	v_mov_b32_e32 v173, 0
	v_cvt_pk_fp8_f32 v173, v154, v155
	v_mul_f32_e32 v157, s58, v125
	v_mul_f32_e32 v154, s58, v129
	v_med3_f32 v155, v157, s56, v153
	v_med3_f32 v154, v154, s56, v153
	v_cvt_pk_fp8_f32 v173, v155, v154 op_sel:[0,0,1]
	ds_write_b128 v137, v[158:161]
	ds_write_b128 v137, v[162:165] offset:128
	ds_write_b128 v137, v[166:169] offset:256
	ds_write_b128 v137, v[170:173] offset:384
	s_waitcnt lgkmcnt(0)
	ds_read_b128 v[158:161], v139
	ds_read_b128 v[162:165], v141
	v_lshl_add_u64 v[154:155], s[0:1], 0, v[134:135]
	v_mad_i64_i32 v[166:167], s[0:1], s26, v136, v[154:155]
	s_waitcnt lgkmcnt(1)
	global_store_dwordx4 v[166:167], v[158:161], off nt
	v_mad_i64_i32 v[166:167], s[0:1], s26, v138, v[154:155]
	ds_read_b128 v[158:161], v143
	s_waitcnt lgkmcnt(1)
	global_store_dwordx4 v[166:167], v[162:165], off nt
	ds_read_b128 v[162:165], v145
	v_mad_i64_i32 v[166:167], s[0:1], s26, v140, v[154:155]
	s_waitcnt lgkmcnt(1)
	global_store_dwordx4 v[166:167], v[158:161], off nt
	v_mad_i64_i32 v[166:167], s[0:1], s26, v142, v[154:155]
	ds_read_b128 v[158:161], v147
	s_waitcnt lgkmcnt(1)
	global_store_dwordx4 v[166:167], v[162:165], off nt
	ds_read_b128 v[162:165], v149
	v_mad_i64_i32 v[166:167], s[0:1], s26, v144, v[154:155]
	s_waitcnt lgkmcnt(1)
	global_store_dwordx4 v[166:167], v[158:161], off nt
	v_mad_i64_i32 v[166:167], s[0:1], s26, v146, v[154:155]
	ds_read_b128 v[158:161], v151
	s_waitcnt lgkmcnt(1)
	global_store_dwordx4 v[166:167], v[162:165], off nt
	ds_read_b128 v[162:165], v152
	v_mad_i64_i32 v[166:167], s[0:1], s26, v148, v[154:155]
	v_mad_i64_i32 v[154:155], s[0:1], s26, v150, v[154:155]
	s_waitcnt lgkmcnt(1)
	global_store_dwordx4 v[166:167], v[158:161], off nt
	s_waitcnt lgkmcnt(0)
	global_store_dwordx4 v[154:155], v[162:165], off nt
	s_waitcnt lgkmcnt(0)
	s_branch .LBB0_830

.LBB0_1272:
	v_mul_u32_u24_e32 v2, s14, v135
	v_lshlrev_b32_e32 v132, 2, v2
	v_lshl_add_u64 v[2:3], s[12:13], 0, v[132:133]
	v_lshlrev_b32_e32 v132, 2, v134
	v_lshl_add_u64 v[2:3], v[2:3], 0, v[132:133]
	s_lshl_b64 s[12:13], s[14:15], 2
	v_lshl_add_u64 v[10:11], v[2:3], 0, s[12:13]
	global_load_dwordx4 v[2:5], v[2:3], off nt
	s_nop 0
	global_load_dwordx4 v[6:9], v[10:11], off nt
	v_lshl_add_u64 v[10:11], v[10:11], 0, s[12:13]
	v_lshl_add_u64 v[18:19], v[10:11], 0, s[12:13]
	global_load_dwordx4 v[10:13], v[10:11], off nt
	s_nop 0
	global_load_dwordx4 v[14:17], v[18:19], off nt
	v_lshl_add_u64 v[18:19], v[18:19], 0, s[12:13]
	v_lshl_add_u64 v[26:27], v[18:19], 0, s[12:13]
	global_load_dwordx4 v[18:21], v[18:19], off nt
	s_nop 0
	global_load_dwordx4 v[22:25], v[26:27], off nt
	v_lshl_add_u64 v[26:27], v[26:27], 0, s[12:13]
	v_lshl_add_u64 v[28:29], v[26:27], 0, s[12:13]
	global_load_dwordx4 v[34:37], v[26:27], off nt
	global_load_dwordx4 v[42:45], v[28:29], off nt
	v_lshl_add_u64 v[26:27], v[28:29], 0, s[12:13]
	v_lshl_add_u64 v[38:39], v[26:27], 0, s[12:13]
	v_lshl_add_u64 v[46:47], v[38:39], 0, s[12:13]
	v_lshl_add_u64 v[50:51], v[46:47], 0, s[12:13]
	v_lshl_add_u64 v[54:55], v[50:51], 0, s[12:13]
	v_lshl_add_u64 v[58:59], v[54:55], 0, s[12:13]
	v_lshl_add_u64 v[62:63], v[58:59], 0, s[12:13]
	global_load_dwordx4 v[30:33], v[26:27], off nt
	s_nop 0
	global_load_dwordx4 v[26:29], v[38:39], off nt
	s_nop 0
	global_load_dwordx4 v[38:41], v[46:47], off nt
	s_nop 0
	global_load_dwordx4 v[46:49], v[50:51], off nt
	s_nop 0
	global_load_dwordx4 v[50:53], v[54:55], off nt
	s_nop 0
	global_load_dwordx4 v[54:57], v[58:59], off nt
	s_nop 0
	global_load_dwordx4 v[58:61], v[62:63], off nt
	v_lshl_add_u64 v[62:63], v[62:63], 0, s[12:13]
	global_load_dwordx4 v[62:65], v[62:63], off nt
	s_branch .Lconv_fast_2

.Lconv_fast_2:
	s_andn2_b64 vcc, exec, s[8:9]
	s_cbranch_vccnz .LBB0_1218
	s_waitcnt vmcnt(31)
	v_mul_f32_e32 v132, s56, v66
	s_waitcnt vmcnt(30)
	v_mul_f32_e32 v158, s56, v70
	v_med3_f32 v132, v132, s47, v157
	v_med3_f32 v160, v158, s47, v157
	v_mov_b32_e32 v158, v133
	v_cvt_pk_fp8_f32 v158, v132, v160
	s_waitcnt vmcnt(29)
	v_mul_f32_e32 v159, s56, v74
	s_waitcnt vmcnt(28)
	v_mul_f32_e32 v132, s56, v78
	v_med3_f32 v159, v159, s47, v157
	v_med3_f32 v132, v132, s47, v157
	v_cvt_pk_fp8_f32 v158, v159, v132 op_sel:[0,0,1]
	s_waitcnt vmcnt(27)
	v_mul_f32_e32 v132, s56, v82
	s_waitcnt vmcnt(26)
	v_mul_f32_e32 v159, s56, v86
	v_med3_f32 v132, v132, s47, v157
	v_med3_f32 v161, v159, s47, v157
	v_mov_b32_e32 v159, v133
	v_cvt_pk_fp8_f32 v159, v132, v161
	s_waitcnt vmcnt(25)
	v_mul_f32_e32 v160, s56, v90
	s_waitcnt vmcnt(24)
	v_mul_f32_e32 v132, s56, v94
	v_med3_f32 v160, v160, s47, v157
	v_med3_f32 v132, v132, s47, v157
	v_cvt_pk_fp8_f32 v159, v160, v132 op_sel:[0,0,1]
	s_waitcnt vmcnt(23)
	v_mul_f32_e32 v132, s56, v98
	s_waitcnt vmcnt(22)
	v_mul_f32_e32 v160, s56, v102
	v_med3_f32 v132, v132, s47, v157
	v_med3_f32 v162, v160, s47, v157
	v_mov_b32_e32 v160, v133
	v_cvt_pk_fp8_f32 v160, v132, v162
	s_waitcnt vmcnt(21)
	v_mul_f32_e32 v161, s56, v106
	s_waitcnt vmcnt(20)
	v_mul_f32_e32 v132, s56, v110
	v_med3_f32 v161, v161, s47, v157
	v_med3_f32 v132, v132, s47, v157
	v_cvt_pk_fp8_f32 v160, v161, v132 op_sel:[0,0,1]
	s_waitcnt vmcnt(19)
	v_mul_f32_e32 v132, s56, v114
	s_waitcnt vmcnt(18)
	v_mul_f32_e32 v161, s56, v118
	v_med3_f32 v132, v132, s47, v157
	v_med3_f32 v163, v161, s47, v157
	v_mov_b32_e32 v161, v133
	v_cvt_pk_fp8_f32 v161, v132, v163
	s_waitcnt vmcnt(17)
	v_mul_f32_e32 v162, s56, v122
	s_waitcnt vmcnt(16)
	v_mul_f32_e32 v132, s56, v126
	v_med3_f32 v162, v162, s47, v157
	v_med3_f32 v132, v132, s47, v157
	v_cvt_pk_fp8_f32 v161, v162, v132 op_sel:[0,0,1]
	v_mul_f32_e32 v132, s56, v67
	v_mul_f32_e32 v162, s56, v71
	v_med3_f32 v132, v132, s47, v157
	v_med3_f32 v164, v162, s47, v157
	v_mov_b32_e32 v162, v133
	v_cvt_pk_fp8_f32 v162, v132, v164
	v_mul_f32_e32 v163, s56, v75
	v_mul_f32_e32 v132, s56, v79
	v_med3_f32 v163, v163, s47, v157
	v_med3_f32 v132, v132, s47, v157
	v_cvt_pk_fp8_f32 v162, v163, v132 op_sel:[0,0,1]
	v_mul_f32_e32 v132, s56, v83
	v_mul_f32_e32 v163, s56, v87
	v_med3_f32 v132, v132, s47, v157
	v_med3_f32 v165, v163, s47, v157
	v_mov_b32_e32 v163, v133
	v_cvt_pk_fp8_f32 v163, v132, v165
	v_mul_f32_e32 v164, s56, v91
	v_mul_f32_e32 v132, s56, v95
	v_med3_f32 v164, v164, s47, v157
	v_med3_f32 v132, v132, s47, v157
	v_cvt_pk_fp8_f32 v163, v164, v132 op_sel:[0,0,1]
	v_mul_f32_e32 v132, s56, v99
	v_mul_f32_e32 v164, s56, v103
	v_med3_f32 v132, v132, s47, v157
	v_med3_f32 v166, v164, s47, v157
	v_mov_b32_e32 v164, v133
	v_cvt_pk_fp8_f32 v164, v132, v166
	v_mul_f32_e32 v165, s56, v107
	v_mul_f32_e32 v132, s56, v111
	v_med3_f32 v165, v165, s47, v157
	v_med3_f32 v132, v132, s47, v157
	v_cvt_pk_fp8_f32 v164, v165, v132 op_sel:[0,0,1]
	v_mul_f32_e32 v132, s56, v115
	v_mul_f32_e32 v165, s56, v119
	v_med3_f32 v132, v132, s47, v157
	v_med3_f32 v167, v165, s47, v157
	v_mov_b32_e32 v165, v133
	v_cvt_pk_fp8_f32 v165, v132, v167
	v_mul_f32_e32 v166, s56, v123
	v_mul_f32_e32 v132, s56, v127
	v_med3_f32 v166, v166, s47, v157
	v_med3_f32 v132, v132, s47, v157
	v_cvt_pk_fp8_f32 v165, v166, v132 op_sel:[0,0,1]
	v_mul_f32_e32 v132, s56, v68
	v_mul_f32_e32 v166, s56, v72
	v_med3_f32 v132, v132, s47, v157
	v_med3_f32 v168, v166, s47, v157
	v_mov_b32_e32 v166, v133
	v_cvt_pk_fp8_f32 v166, v132, v168
	v_mul_f32_e32 v167, s56, v76
	v_mul_f32_e32 v132, s56, v80
	v_med3_f32 v167, v167, s47, v157
	v_med3_f32 v132, v132, s47, v157
	v_cvt_pk_fp8_f32 v166, v167, v132 op_sel:[0,0,1]
	v_mul_f32_e32 v132, s56, v84
	v_mul_f32_e32 v167, s56, v88
	v_med3_f32 v132, v132, s47, v157
	v_med3_f32 v169, v167, s47, v157
	v_mov_b32_e32 v167, v133
	v_cvt_pk_fp8_f32 v167, v132, v169
	v_mul_f32_e32 v168, s56, v92
	v_mul_f32_e32 v132, s56, v96
	v_med3_f32 v168, v168, s47, v157
	v_med3_f32 v132, v132, s47, v157
	v_cvt_pk_fp8_f32 v167, v168, v132 op_sel:[0,0,1]
	v_mul_f32_e32 v132, s56, v100
	v_mul_f32_e32 v168, s56, v104
	v_med3_f32 v132, v132, s47, v157
	v_med3_f32 v170, v168, s47, v157
	v_mov_b32_e32 v168, v133
	v_cvt_pk_fp8_f32 v168, v132, v170
	v_mul_f32_e32 v169, s56, v108
	v_mul_f32_e32 v132, s56, v112
	v_med3_f32 v169, v169, s47, v157
	v_med3_f32 v132, v132, s47, v157
	v_cvt_pk_fp8_f32 v168, v169, v132 op_sel:[0,0,1]
	v_mul_f32_e32 v132, s56, v116
	v_mul_f32_e32 v169, s56, v120
	v_med3_f32 v132, v132, s47, v157
	v_med3_f32 v171, v169, s47, v157
	v_mov_b32_e32 v169, v133
	v_cvt_pk_fp8_f32 v169, v132, v171
	v_mul_f32_e32 v170, s56, v124
	v_mul_f32_e32 v132, s56, v128
	v_med3_f32 v170, v170, s47, v157
	v_med3_f32 v132, v132, s47, v157
	v_cvt_pk_fp8_f32 v169, v170, v132 op_sel:[0,0,1]
	v_mul_f32_e32 v132, s56, v69
	v_mul_f32_e32 v170, s56, v73
	v_med3_f32 v132, v132, s47, v157
	v_med3_f32 v172, v170, s47, v157
	v_mov_b32_e32 v170, v133
	v_cvt_pk_fp8_f32 v170, v132, v172
	v_mul_f32_e32 v171, s56, v77
	v_mul_f32_e32 v132, s56, v81
	v_med3_f32 v171, v171, s47, v157
	v_med3_f32 v132, v132, s47, v157
	v_cvt_pk_fp8_f32 v170, v171, v132 op_sel:[0,0,1]
	v_mul_f32_e32 v132, s56, v85
	v_mul_f32_e32 v171, s56, v89
	v_med3_f32 v132, v132, s47, v157
	v_med3_f32 v173, v171, s47, v157
	v_mov_b32_e32 v171, v133
	v_cvt_pk_fp8_f32 v171, v132, v173
	v_mul_f32_e32 v172, s56, v93
	v_mul_f32_e32 v132, s56, v97
	v_med3_f32 v172, v172, s47, v157
	v_med3_f32 v132, v132, s47, v157
	v_cvt_pk_fp8_f32 v171, v172, v132 op_sel:[0,0,1]
	v_mul_f32_e32 v132, s56, v101
	v_mul_f32_e32 v172, s56, v105
	v_med3_f32 v132, v132, s47, v157
	v_med3_f32 v174, v172, s47, v157
	v_mov_b32_e32 v172, v133
	v_cvt_pk_fp8_f32 v172, v132, v174
	v_mul_f32_e32 v173, s56, v109
	v_mul_f32_e32 v132, s56, v113
	v_med3_f32 v173, v173, s47, v157
	v_med3_f32 v132, v132, s47, v157
	v_cvt_pk_fp8_f32 v172, v173, v132 op_sel:[0,0,1]
	v_mul_f32_e32 v132, s56, v117
	v_mul_f32_e32 v173, s56, v121
	v_med3_f32 v132, v132, s47, v157
	v_med3_f32 v175, v173, s47, v157
	v_mov_b32_e32 v173, v133
	v_cvt_pk_fp8_f32 v173, v132, v175
	v_mul_f32_e32 v174, s56, v125
	v_mul_f32_e32 v132, s56, v129
	v_med3_f32 v174, v174, s47, v157
	v_med3_f32 v132, v132, s47, v157
	v_cvt_pk_fp8_f32 v173, v174, v132 op_sel:[0,0,1]
	ds_write_b128 v143, v[158:161]
	ds_write_b128 v143, v[162:165] offset:128
	ds_write_b128 v143, v[166:169] offset:256
	ds_write_b128 v143, v[170:173] offset:384
	s_waitcnt lgkmcnt(0)
	ds_read_b128 v[158:161], v145
	ds_read_b128 v[162:165], v147
	v_lshl_add_u64 v[166:167], s[0:1], 0, v[136:137]
	v_mad_i64_i32 v[168:169], s[0:1], s25, v130, v[166:167]
	s_waitcnt lgkmcnt(1)
	global_store_dwordx4 v[168:169], v[158:161], off nt
	v_mad_i64_i32 v[168:169], s[0:1], s25, v138, v[166:167]
	ds_read_b128 v[158:161], v149
	s_waitcnt lgkmcnt(1)
	global_store_dwordx4 v[168:169], v[162:165], off nt
	ds_read_b128 v[162:165], v151
	v_mad_i64_i32 v[168:169], s[0:1], s25, v140, v[166:167]
	s_waitcnt lgkmcnt(1)
	global_store_dwordx4 v[168:169], v[158:161], off nt
	v_mad_i64_i32 v[168:169], s[0:1], s25, v142, v[166:167]
	ds_read_b128 v[158:161], v152
	s_waitcnt lgkmcnt(1)
	global_store_dwordx4 v[168:169], v[162:165], off nt
	ds_read_b128 v[162:165], v153
	v_mad_i64_i32 v[168:169], s[0:1], s25, v144, v[166:167]
	s_waitcnt lgkmcnt(1)
	global_store_dwordx4 v[168:169], v[158:161], off nt
	v_mad_i64_i32 v[168:169], s[0:1], s25, v146, v[166:167]
	ds_read_b128 v[158:161], v154
	s_waitcnt lgkmcnt(1)
	global_store_dwordx4 v[168:169], v[162:165], off nt
	ds_read_b128 v[162:165], v155
	v_mad_i64_i32 v[168:169], s[0:1], s25, v148, v[166:167]
	s_waitcnt lgkmcnt(1)
	global_store_dwordx4 v[168:169], v[158:161], off nt
	s_nop 1
	v_mad_i64_i32 v[158:159], s[0:1], s25, v150, v[166:167]
	s_waitcnt lgkmcnt(0)
	global_store_dwordx4 v[158:159], v[162:165], off nt
	s_waitcnt lgkmcnt(0)
	s_branch .LBB0_1218

.LBB0_1367:
	v_mul_hi_i32_i24_e32 v3, s12, v132
	v_mul_i32_i24_e32 v2, s12, v132
	v_lshl_add_u64 v[2:3], v[2:3], 2, s[10:11]
	v_lshl_add_u64 v[2:3], v[134:135], 2, v[2:3]
	s_lshl_b64 s[10:11], s[12:13], 2
	v_lshl_add_u64 v[10:11], v[2:3], 0, s[10:11]
	global_load_dwordx4 v[2:5], v[2:3], off nt
	s_nop 0
	global_load_dwordx4 v[6:9], v[10:11], off nt
	v_lshl_add_u64 v[10:11], v[10:11], 0, s[10:11]
	v_lshl_add_u64 v[18:19], v[10:11], 0, s[10:11]
	global_load_dwordx4 v[10:13], v[10:11], off nt
	s_nop 0
	global_load_dwordx4 v[14:17], v[18:19], off nt
	v_lshl_add_u64 v[18:19], v[18:19], 0, s[10:11]
	v_lshl_add_u64 v[26:27], v[18:19], 0, s[10:11]
	global_load_dwordx4 v[18:21], v[18:19], off nt
	s_nop 0
	global_load_dwordx4 v[22:25], v[26:27], off nt
	v_lshl_add_u64 v[26:27], v[26:27], 0, s[10:11]
	v_lshl_add_u64 v[28:29], v[26:27], 0, s[10:11]
	global_load_dwordx4 v[34:37], v[26:27], off nt
	global_load_dwordx4 v[42:45], v[28:29], off nt
	v_lshl_add_u64 v[26:27], v[28:29], 0, s[10:11]
	v_lshl_add_u64 v[38:39], v[26:27], 0, s[10:11]
	v_lshl_add_u64 v[46:47], v[38:39], 0, s[10:11]
	v_lshl_add_u64 v[50:51], v[46:47], 0, s[10:11]
	v_lshl_add_u64 v[54:55], v[50:51], 0, s[10:11]
	v_lshl_add_u64 v[58:59], v[54:55], 0, s[10:11]
	v_lshl_add_u64 v[62:63], v[58:59], 0, s[10:11]
	global_load_dwordx4 v[30:33], v[26:27], off nt
	s_nop 0
	global_load_dwordx4 v[26:29], v[38:39], off nt
	s_nop 0
	global_load_dwordx4 v[38:41], v[46:47], off nt
	s_nop 0
	global_load_dwordx4 v[46:49], v[50:51], off nt
	s_nop 0
	global_load_dwordx4 v[50:53], v[54:55], off nt
	s_nop 0
	global_load_dwordx4 v[54:57], v[58:59], off nt
	s_nop 0
	global_load_dwordx4 v[58:61], v[62:63], off nt
	v_lshl_add_u64 v[62:63], v[62:63], 0, s[10:11]
	global_load_dwordx4 v[62:65], v[62:63], off nt
	s_branch .Lconv_fast_5

.Lconv_fast_5:
	s_andn2_b64 vcc, exec, s[6:7]
	s_cbranch_vccnz .LBB0_1313
	s_waitcnt vmcnt(31)
	v_mul_f32_e32 v155, s45, v66
	s_waitcnt vmcnt(30)
	v_mul_f32_e32 v157, s45, v70
	v_med3_f32 v155, v155, s43, v154
	v_med3_f32 v157, v157, s43, v154
	v_mov_b32_e32 v158, 0
	v_cvt_pk_fp8_f32 v158, v155, v157
	s_waitcnt vmcnt(29)
	v_mul_f32_e32 v159, s45, v74
	s_waitcnt vmcnt(28)
	v_mul_f32_e32 v155, s45, v78
	v_med3_f32 v157, v159, s43, v154
	v_med3_f32 v155, v155, s43, v154
	v_cvt_pk_fp8_f32 v158, v157, v155 op_sel:[0,0,1]
	s_waitcnt vmcnt(27)
	v_mul_f32_e32 v155, s45, v82
	s_waitcnt vmcnt(26)
	v_mul_f32_e32 v157, s45, v86
	v_med3_f32 v155, v155, s43, v154
	v_med3_f32 v157, v157, s43, v154
	v_mov_b32_e32 v159, 0
	v_cvt_pk_fp8_f32 v159, v155, v157
	s_waitcnt vmcnt(25)
	v_mul_f32_e32 v160, s45, v90
	s_waitcnt vmcnt(24)
	v_mul_f32_e32 v155, s45, v94
	v_med3_f32 v157, v160, s43, v154
	v_med3_f32 v155, v155, s43, v154
	v_cvt_pk_fp8_f32 v159, v157, v155 op_sel:[0,0,1]
	s_waitcnt vmcnt(23)
	v_mul_f32_e32 v155, s45, v98
	s_waitcnt vmcnt(22)
	v_mul_f32_e32 v157, s45, v102
	v_med3_f32 v155, v155, s43, v154
	v_med3_f32 v157, v157, s43, v154
	v_mov_b32_e32 v160, 0
	v_cvt_pk_fp8_f32 v160, v155, v157
	s_waitcnt vmcnt(21)
	v_mul_f32_e32 v161, s45, v106
	s_waitcnt vmcnt(20)
	v_mul_f32_e32 v155, s45, v110
	v_med3_f32 v157, v161, s43, v154
	v_med3_f32 v155, v155, s43, v154
	v_cvt_pk_fp8_f32 v160, v157, v155 op_sel:[0,0,1]
	s_waitcnt vmcnt(19)
	v_mul_f32_e32 v155, s45, v114
	s_waitcnt vmcnt(18)
	v_mul_f32_e32 v157, s45, v118
	v_med3_f32 v155, v155, s43, v154
	v_med3_f32 v157, v157, s43, v154
	v_mov_b32_e32 v161, 0
	v_cvt_pk_fp8_f32 v161, v155, v157
	s_waitcnt vmcnt(17)
	v_mul_f32_e32 v162, s45, v122
	s_waitcnt vmcnt(16)
	v_mul_f32_e32 v155, s45, v126
	v_med3_f32 v157, v162, s43, v154
	v_med3_f32 v155, v155, s43, v154
	v_cvt_pk_fp8_f32 v161, v157, v155 op_sel:[0,0,1]
	v_mul_f32_e32 v155, s45, v67
	v_mul_f32_e32 v157, s45, v71
	v_med3_f32 v155, v155, s43, v154
	v_med3_f32 v157, v157, s43, v154
	v_mov_b32_e32 v162, 0
	v_cvt_pk_fp8_f32 v162, v155, v157
	v_mul_f32_e32 v163, s45, v75
	v_mul_f32_e32 v155, s45, v79
	v_med3_f32 v157, v163, s43, v154
	v_med3_f32 v155, v155, s43, v154
	v_cvt_pk_fp8_f32 v162, v157, v155 op_sel:[0,0,1]
	v_mul_f32_e32 v155, s45, v83
	v_mul_f32_e32 v157, s45, v87
	v_med3_f32 v155, v155, s43, v154
	v_med3_f32 v157, v157, s43, v154
	v_mov_b32_e32 v163, 0
	v_cvt_pk_fp8_f32 v163, v155, v157
	v_mul_f32_e32 v164, s45, v91
	v_mul_f32_e32 v155, s45, v95
	v_med3_f32 v157, v164, s43, v154
	v_med3_f32 v155, v155, s43, v154
	v_cvt_pk_fp8_f32 v163, v157, v155 op_sel:[0,0,1]
	v_mul_f32_e32 v155, s45, v99
	v_mul_f32_e32 v157, s45, v103
	v_med3_f32 v155, v155, s43, v154
	v_med3_f32 v157, v157, s43, v154
	v_mov_b32_e32 v164, 0
	v_cvt_pk_fp8_f32 v164, v155, v157
	v_mul_f32_e32 v165, s45, v107
	v_mul_f32_e32 v155, s45, v111
	v_med3_f32 v157, v165, s43, v154
	v_med3_f32 v155, v155, s43, v154
	v_cvt_pk_fp8_f32 v164, v157, v155 op_sel:[0,0,1]
	v_mul_f32_e32 v155, s45, v115
	v_mul_f32_e32 v157, s45, v119
	v_med3_f32 v155, v155, s43, v154
	v_med3_f32 v157, v157, s43, v154
	v_mov_b32_e32 v165, 0
	v_cvt_pk_fp8_f32 v165, v155, v157
	v_mul_f32_e32 v166, s45, v123
	v_mul_f32_e32 v155, s45, v127
	v_med3_f32 v157, v166, s43, v154
	v_med3_f32 v155, v155, s43, v154
	v_cvt_pk_fp8_f32 v165, v157, v155 op_sel:[0,0,1]
	v_mul_f32_e32 v155, s45, v68
	v_mul_f32_e32 v157, s45, v72
	v_med3_f32 v155, v155, s43, v154
	v_med3_f32 v157, v157, s43, v154
	v_mov_b32_e32 v166, 0
	v_cvt_pk_fp8_f32 v166, v155, v157
	v_mul_f32_e32 v167, s45, v76
	v_mul_f32_e32 v155, s45, v80
	v_med3_f32 v157, v167, s43, v154
	v_med3_f32 v155, v155, s43, v154
	v_cvt_pk_fp8_f32 v166, v157, v155 op_sel:[0,0,1]
	v_mul_f32_e32 v155, s45, v84
	v_mul_f32_e32 v157, s45, v88
	v_med3_f32 v155, v155, s43, v154
	v_med3_f32 v157, v157, s43, v154
	v_mov_b32_e32 v167, 0
	v_cvt_pk_fp8_f32 v167, v155, v157
	v_mul_f32_e32 v168, s45, v92
	v_mul_f32_e32 v155, s45, v96
	v_med3_f32 v157, v168, s43, v154
	v_med3_f32 v155, v155, s43, v154
	v_cvt_pk_fp8_f32 v167, v157, v155 op_sel:[0,0,1]
	v_mul_f32_e32 v155, s45, v100
	v_mul_f32_e32 v157, s45, v104
	v_med3_f32 v155, v155, s43, v154
	v_med3_f32 v157, v157, s43, v154
	v_mov_b32_e32 v168, 0
	v_cvt_pk_fp8_f32 v168, v155, v157
	v_mul_f32_e32 v169, s45, v108
	v_mul_f32_e32 v155, s45, v112
	v_med3_f32 v157, v169, s43, v154
	v_med3_f32 v155, v155, s43, v154
	v_cvt_pk_fp8_f32 v168, v157, v155 op_sel:[0,0,1]
	v_mul_f32_e32 v155, s45, v116
	v_mul_f32_e32 v157, s45, v120
	v_med3_f32 v155, v155, s43, v154
	v_med3_f32 v157, v157, s43, v154
	v_mov_b32_e32 v169, 0
	v_cvt_pk_fp8_f32 v169, v155, v157
	v_mul_f32_e32 v170, s45, v124
	v_mul_f32_e32 v155, s45, v128
	v_med3_f32 v157, v170, s43, v154
	v_med3_f32 v155, v155, s43, v154
	v_cvt_pk_fp8_f32 v169, v157, v155 op_sel:[0,0,1]
	v_mul_f32_e32 v155, s45, v69
	v_mul_f32_e32 v157, s45, v73
	v_med3_f32 v155, v155, s43, v154
	v_med3_f32 v157, v157, s43, v154
	v_mov_b32_e32 v170, 0
	v_cvt_pk_fp8_f32 v170, v155, v157
	v_mul_f32_e32 v171, s45, v77
	v_mul_f32_e32 v155, s45, v81
	v_med3_f32 v157, v171, s43, v154
	v_med3_f32 v155, v155, s43, v154
	v_cvt_pk_fp8_f32 v170, v157, v155 op_sel:[0,0,1]
	v_mul_f32_e32 v155, s45, v85
	v_mul_f32_e32 v157, s45, v89
	v_med3_f32 v155, v155, s43, v154
	v_med3_f32 v157, v157, s43, v154
	v_mov_b32_e32 v171, 0
	v_cvt_pk_fp8_f32 v171, v155, v157
	v_mul_f32_e32 v172, s45, v93
	v_mul_f32_e32 v155, s45, v97
	v_med3_f32 v157, v172, s43, v154
	v_med3_f32 v155, v155, s43, v154
	v_cvt_pk_fp8_f32 v171, v157, v155 op_sel:[0,0,1]
	v_mul_f32_e32 v155, s45, v101
	v_mul_f32_e32 v157, s45, v105
	v_med3_f32 v155, v155, s43, v154
	v_med3_f32 v157, v157, s43, v154
	v_mov_b32_e32 v172, 0
	v_cvt_pk_fp8_f32 v172, v155, v157
	v_mul_f32_e32 v173, s45, v109
	v_mul_f32_e32 v155, s45, v113
	v_med3_f32 v157, v173, s43, v154
	v_med3_f32 v155, v155, s43, v154
	v_cvt_pk_fp8_f32 v172, v157, v155 op_sel:[0,0,1]
	v_mul_f32_e32 v155, s45, v117
	v_mul_f32_e32 v157, s45, v121
	v_med3_f32 v155, v155, s43, v154
	v_med3_f32 v157, v157, s43, v154
	v_mov_b32_e32 v173, 0
	v_cvt_pk_fp8_f32 v173, v155, v157
	v_mul_f32_e32 v174, s45, v125
	v_mul_f32_e32 v155, s45, v129
	v_med3_f32 v157, v174, s43, v154
	v_med3_f32 v155, v155, s43, v154
	v_cvt_pk_fp8_f32 v173, v157, v155 op_sel:[0,0,1]
	ds_write_b128 v139, v[158:161]
	ds_write_b128 v139, v[162:165] offset:128
	ds_write_b128 v139, v[166:169] offset:256
	ds_write_b128 v139, v[170:173] offset:384
	s_waitcnt lgkmcnt(0)
	ds_read_b128 v[158:161], v141
	ds_read_b128 v[162:165], v143
	v_lshl_add_u64 v[166:167], s[0:1], 0, v[136:137]
	v_mad_i64_i32 v[168:169], s[0:1], s17, v130, v[166:167]
	s_waitcnt lgkmcnt(1)
	global_store_dwordx4 v[168:169], v[158:161], off nt
	v_mad_i64_i32 v[168:169], s[0:1], s17, v138, v[166:167]
	ds_read_b128 v[158:161], v145
	s_waitcnt lgkmcnt(1)
	global_store_dwordx4 v[168:169], v[162:165], off nt
	ds_read_b128 v[162:165], v147
	v_mad_i64_i32 v[168:169], s[0:1], s17, v140, v[166:167]
	s_waitcnt lgkmcnt(1)
	global_store_dwordx4 v[168:169], v[158:161], off nt
	v_mad_i64_i32 v[168:169], s[0:1], s17, v142, v[166:167]
	ds_read_b128 v[158:161], v149
	s_waitcnt lgkmcnt(1)
	global_store_dwordx4 v[168:169], v[162:165], off nt
	ds_read_b128 v[162:165], v151
	v_mad_i64_i32 v[168:169], s[0:1], s17, v144, v[166:167]
	s_waitcnt lgkmcnt(1)
	global_store_dwordx4 v[168:169], v[158:161], off nt
	v_mad_i64_i32 v[168:169], s[0:1], s17, v146, v[166:167]
	ds_read_b128 v[158:161], v152
	s_waitcnt lgkmcnt(1)
	global_store_dwordx4 v[168:169], v[162:165], off nt
	ds_read_b128 v[162:165], v153
	v_mad_i64_i32 v[168:169], s[0:1], s17, v148, v[166:167]
	s_waitcnt lgkmcnt(1)
	global_store_dwordx4 v[168:169], v[158:161], off nt
	s_nop 1
	v_mad_i64_i32 v[158:159], s[0:1], s17, v150, v[166:167]
	s_waitcnt lgkmcnt(0)
	global_store_dwordx4 v[158:159], v[162:165], off nt
	s_waitcnt lgkmcnt(0)
	s_branch .LBB0_1313
